# speedup vs baseline: 1.0199x; 1.0037x over previous
.Lk_first:
	ds_read_b128 v[130:133], v219 offset:32768
	ds_read_b128 v[134:137], v219 offset:33792
	ds_read_b128 v[138:141], v219 offset:34816
	ds_read_b128 v[142:145], v219 offset:35840
	ds_read_b128 v[178:181], v219 offset:49152
	ds_read_b128 v[182:185], v219 offset:50176
	ds_read_b128 v[186:189], v219 offset:51200
	ds_read_b128 v[190:193], v219 offset:52224
	ds_read_b128 v[146:149], v220
	ds_read_b128 v[150:153], v220 offset:1024
	ds_read_b128 v[154:157], v221
	ds_read_b128 v[158:161], v221 offset:1024
	ds_read_b128 v[162:165], v222
	ds_read_b128 v[166:169], v222 offset:1024
	ds_read_b128 v[170:173], v223
	ds_read_b128 v[174:177], v223 offset:1024
	s_add_i32 s12, s8, 1
	s_mov_b32 m0, s43
	v_readlane_b32 s9, v248, s12
	s_nop 1
	v_add_u32_e32 v251, s9, v249
	global_load_lds_dwordx4 v251, s[18:19]
	v_add_u32_e32 v251, s9, v250
	s_mov_b32 m0, s44
	s_nop 0
	global_load_lds_dwordx4 v251, s[18:19]
	s_waitcnt lgkmcnt(0)
	s_barrier
	s_setprio 1
	v_mfma_f32_16x16x32_f16 v[124:127], v[130:133], v[146:149], 0
	v_mfma_f32_16x16x32_f16 v[124:127], v[134:137], v[150:153], v[124:127]
	v_mfma_f32_16x16x32_f16 v[120:123], v[138:141], v[146:149], 0
	v_mfma_f32_16x16x32_f16 v[120:123], v[142:145], v[150:153], v[120:123]
	v_mfma_f32_16x16x32_f16 v[52:55], v[178:181], v[146:149], 0
	v_mfma_f32_16x16x32_f16 v[52:55], v[182:185], v[150:153], v[52:55]
	v_mfma_f32_16x16x32_f16 v[40:43], v[186:189], v[146:149], 0
	v_mfma_f32_16x16x32_f16 v[40:43], v[190:193], v[150:153], v[40:43]
	v_mfma_f32_16x16x32_f16 v[116:119], v[130:133], v[154:157], 0
	v_mfma_f32_16x16x32_f16 v[116:119], v[134:137], v[158:161], v[116:119]
	v_mfma_f32_16x16x32_f16 v[112:115], v[138:141], v[154:157], 0
	v_mfma_f32_16x16x32_f16 v[112:115], v[142:145], v[158:161], v[112:115]
	v_mfma_f32_16x16x32_f16 v[36:39], v[178:181], v[154:157], 0
	v_mfma_f32_16x16x32_f16 v[36:39], v[182:185], v[158:161], v[36:39]
	v_mfma_f32_16x16x32_f16 v[32:35], v[186:189], v[154:157], 0
	v_mfma_f32_16x16x32_f16 v[32:35], v[190:193], v[158:161], v[32:35]
	v_mfma_f32_16x16x32_f16 v[108:111], v[130:133], v[162:165], 0
	v_mfma_f32_16x16x32_f16 v[108:111], v[134:137], v[166:169], v[108:111]
	v_mfma_f32_16x16x32_f16 v[104:107], v[138:141], v[162:165], 0
	v_mfma_f32_16x16x32_f16 v[104:107], v[142:145], v[166:169], v[104:107]
	v_mfma_f32_16x16x32_f16 v[28:31], v[178:181], v[162:165], 0
	v_mfma_f32_16x16x32_f16 v[28:31], v[182:185], v[166:169], v[28:31]
	v_mfma_f32_16x16x32_f16 v[24:27], v[186:189], v[162:165], 0
	v_mfma_f32_16x16x32_f16 v[24:27], v[190:193], v[166:169], v[24:27]
	v_mfma_f32_16x16x32_f16 v[100:103], v[130:133], v[170:173], 0
	v_mfma_f32_16x16x32_f16 v[100:103], v[134:137], v[174:177], v[100:103]
	v_mfma_f32_16x16x32_f16 v[96:99], v[138:141], v[170:173], 0
	v_mfma_f32_16x16x32_f16 v[96:99], v[142:145], v[174:177], v[96:99]
	v_mfma_f32_16x16x32_f16 v[20:23], v[178:181], v[170:173], 0
	v_mfma_f32_16x16x32_f16 v[20:23], v[182:185], v[174:177], v[20:23]
	v_mfma_f32_16x16x32_f16 v[16:19], v[186:189], v[170:173], 0
	v_mfma_f32_16x16x32_f16 v[16:19], v[190:193], v[174:177], v[16:19]
	s_setprio 0
	s_barrier
	ds_read_b128 v[146:149], v220 offset:16384
	ds_read_b128 v[150:153], v220 offset:17408
	ds_read_b128 v[154:157], v221 offset:16384
	ds_read_b128 v[158:161], v221 offset:17408
	ds_read_b128 v[162:165], v222 offset:16384
	ds_read_b128 v[166:169], v222 offset:17408
	ds_read_b128 v[170:173], v223 offset:16384
	ds_read_b128 v[174:177], v223 offset:17408
	v_add_u32_e32 v129, s7, v128
	s_mov_b32 m0, s22
	v_add_u32_e32 v194, 0xffffff80, v129
	global_load_lds_dwordx4 v194, s[10:11]
	v_add_u32_e32 v194, 0x47f80, v129
	s_mov_b32 m0, s23
	s_add_i32 s9, s8, 2
	global_load_lds_dwordx4 v194, s[10:11]
	v_readlane_b32 s13, v248, s9
	s_mov_b32 m0, s21
	s_nop 1
	v_add_u32_e32 v194, s13, v206
	global_load_lds_dwordx4 v194, s[18:19]
	v_add_u32_e32 v194, s13, v213
	s_mov_b32 m0, s24
	s_nop 0
	global_load_lds_dwordx4 v194, s[18:19]
	s_mov_b32 m0, s25
	v_add_u32_e32 v194, 0x8ff80, v129
	global_load_lds_dwordx4 v194, s[10:11]
	v_add_u32_e32 v194, 0xd7f80, v129
	s_mov_b32 m0, s26
	s_nop 0
	global_load_lds_dwordx4 v194, s[10:11]
	s_waitcnt vmcnt(8) lgkmcnt(0)
	s_barrier
	s_setprio 1
	v_mfma_f32_16x16x32_f16 v[12:15], v[130:133], v[146:149], 0
	v_mfma_f32_16x16x32_f16 v[12:15], v[134:137], v[150:153], v[12:15]
	v_mfma_f32_16x16x32_f16 v[8:11], v[138:141], v[146:149], 0
	v_mfma_f32_16x16x32_f16 v[8:11], v[142:145], v[150:153], v[8:11]
	v_mfma_f32_16x16x32_f16 v[64:67], v[178:181], v[146:149], 0
	v_mfma_f32_16x16x32_f16 v[64:67], v[182:185], v[150:153], v[64:67]
	v_mfma_f32_16x16x32_f16 v[68:71], v[186:189], v[146:149], 0
	v_mfma_f32_16x16x32_f16 v[68:71], v[190:193], v[150:153], v[68:71]
	v_mfma_f32_16x16x32_f16 v[4:7], v[130:133], v[154:157], 0
	v_mfma_f32_16x16x32_f16 v[4:7], v[134:137], v[158:161], v[4:7]
	v_mfma_f32_16x16x32_f16 v[0:3], v[138:141], v[154:157], 0
	v_mfma_f32_16x16x32_f16 v[0:3], v[142:145], v[158:161], v[0:3]
	v_mfma_f32_16x16x32_f16 v[72:75], v[178:181], v[154:157], 0
	v_mfma_f32_16x16x32_f16 v[72:75], v[182:185], v[158:161], v[72:75]
	v_mfma_f32_16x16x32_f16 v[76:79], v[186:189], v[154:157], 0
	v_mfma_f32_16x16x32_f16 v[76:79], v[190:193], v[158:161], v[76:79]
	v_mfma_f32_16x16x32_f16 v[44:47], v[130:133], v[162:165], 0
	v_mfma_f32_16x16x32_f16 v[44:47], v[134:137], v[166:169], v[44:47]
	v_mfma_f32_16x16x32_f16 v[48:51], v[138:141], v[162:165], 0
	v_mfma_f32_16x16x32_f16 v[48:51], v[142:145], v[166:169], v[48:51]
	v_mfma_f32_16x16x32_f16 v[80:83], v[178:181], v[162:165], 0
	v_mfma_f32_16x16x32_f16 v[80:83], v[182:185], v[166:169], v[80:83]
	v_mfma_f32_16x16x32_f16 v[84:87], v[186:189], v[162:165], 0
	v_mfma_f32_16x16x32_f16 v[84:87], v[190:193], v[166:169], v[84:87]
	v_mfma_f32_16x16x32_f16 v[56:59], v[130:133], v[170:173], 0
	v_mfma_f32_16x16x32_f16 v[56:59], v[134:137], v[174:177], v[56:59]
	v_mfma_f32_16x16x32_f16 v[60:63], v[138:141], v[170:173], 0
	v_mfma_f32_16x16x32_f16 v[60:63], v[142:145], v[174:177], v[60:63]
	v_mfma_f32_16x16x32_f16 v[88:91], v[178:181], v[170:173], 0
	v_mfma_f32_16x16x32_f16 v[88:91], v[182:185], v[174:177], v[88:91]
	v_mfma_f32_16x16x32_f16 v[92:95], v[186:189], v[170:173], 0
	v_mfma_f32_16x16x32_f16 v[92:95], v[190:193], v[174:177], v[92:95]
	s_setprio 0
	s_barrier
	ds_read_b128 v[130:133], v224
	ds_read_b128 v[134:137], v224 offset:1024
	ds_read_b128 v[138:141], v224 offset:2048
	ds_read_b128 v[142:145], v224 offset:3072
	ds_read_b128 v[178:181], v229
	ds_read_b128 v[182:185], v229 offset:1024
	ds_read_b128 v[186:189], v229 offset:2048
	ds_read_b128 v[190:193], v229 offset:3072
	ds_read_b128 v[146:149], v225
	ds_read_b128 v[150:153], v225 offset:1024
	ds_read_b128 v[154:157], v226
	ds_read_b128 v[158:161], v226 offset:1024
	ds_read_b128 v[162:165], v227
	ds_read_b128 v[166:169], v227 offset:1024
	ds_read_b128 v[170:173], v228
	ds_read_b128 v[174:177], v228 offset:1024
	v_readlane_b32 s12, v248, s9
	s_mov_b32 m0, s27
	s_nop 1
	v_add_u32_e32 v251, s12, v249
	global_load_lds_dwordx4 v251, s[18:19]
	v_add_u32_e32 v251, s12, v250
	s_mov_b32 m0, s28
	s_nop 0
	global_load_lds_dwordx4 v251, s[18:19]
	s_waitcnt vmcnt(8) lgkmcnt(0)
	s_barrier
	s_setprio 1
	v_mfma_f32_16x16x32_f16 v[124:127], v[130:133], v[146:149], v[124:127]
	v_mfma_f32_16x16x32_f16 v[124:127], v[134:137], v[150:153], v[124:127]
	v_mfma_f32_16x16x32_f16 v[120:123], v[138:141], v[146:149], v[120:123]
	v_mfma_f32_16x16x32_f16 v[120:123], v[142:145], v[150:153], v[120:123]
	v_mfma_f32_16x16x32_f16 v[52:55], v[178:181], v[146:149], v[52:55]
	v_mfma_f32_16x16x32_f16 v[52:55], v[182:185], v[150:153], v[52:55]
	v_mfma_f32_16x16x32_f16 v[40:43], v[186:189], v[146:149], v[40:43]
	v_mfma_f32_16x16x32_f16 v[40:43], v[190:193], v[150:153], v[40:43]
	v_mfma_f32_16x16x32_f16 v[116:119], v[130:133], v[154:157], v[116:119]
	v_mfma_f32_16x16x32_f16 v[116:119], v[134:137], v[158:161], v[116:119]
	v_mfma_f32_16x16x32_f16 v[112:115], v[138:141], v[154:157], v[112:115]
	v_mfma_f32_16x16x32_f16 v[112:115], v[142:145], v[158:161], v[112:115]
	v_mfma_f32_16x16x32_f16 v[36:39], v[178:181], v[154:157], v[36:39]
	v_mfma_f32_16x16x32_f16 v[36:39], v[182:185], v[158:161], v[36:39]
	v_mfma_f32_16x16x32_f16 v[32:35], v[186:189], v[154:157], v[32:35]
	v_mfma_f32_16x16x32_f16 v[32:35], v[190:193], v[158:161], v[32:35]
	v_mfma_f32_16x16x32_f16 v[108:111], v[130:133], v[162:165], v[108:111]
	v_mfma_f32_16x16x32_f16 v[108:111], v[134:137], v[166:169], v[108:111]
	v_mfma_f32_16x16x32_f16 v[104:107], v[138:141], v[162:165], v[104:107]
	v_mfma_f32_16x16x32_f16 v[104:107], v[142:145], v[166:169], v[104:107]
	v_mfma_f32_16x16x32_f16 v[28:31], v[178:181], v[162:165], v[28:31]
	v_mfma_f32_16x16x32_f16 v[28:31], v[182:185], v[166:169], v[28:31]
	v_mfma_f32_16x16x32_f16 v[24:27], v[186:189], v[162:165], v[24:27]
	v_mfma_f32_16x16x32_f16 v[24:27], v[190:193], v[166:169], v[24:27]
	v_mfma_f32_16x16x32_f16 v[100:103], v[130:133], v[170:173], v[100:103]
	v_mfma_f32_16x16x32_f16 v[100:103], v[134:137], v[174:177], v[100:103]
	v_mfma_f32_16x16x32_f16 v[96:99], v[138:141], v[170:173], v[96:99]
	v_mfma_f32_16x16x32_f16 v[96:99], v[142:145], v[174:177], v[96:99]
	v_mfma_f32_16x16x32_f16 v[20:23], v[178:181], v[170:173], v[20:23]
	v_mfma_f32_16x16x32_f16 v[20:23], v[182:185], v[174:177], v[20:23]
	v_mfma_f32_16x16x32_f16 v[16:19], v[186:189], v[170:173], v[16:19]
	v_mfma_f32_16x16x32_f16 v[16:19], v[190:193], v[174:177], v[16:19]
	s_setprio 0
	s_barrier
	ds_read_b128 v[146:149], v230
	ds_read_b128 v[150:153], v230 offset:1024
	ds_read_b128 v[154:157], v231
	ds_read_b128 v[158:161], v231 offset:1024
	ds_read_b128 v[162:165], v232
	ds_read_b128 v[166:169], v232 offset:1024
	ds_read_b128 v[170:173], v233
	ds_read_b128 v[174:177], v233 offset:1024
	s_mov_b32 m0, s37
	v_add_u32_e32 v194, 0x48000, v129
	global_load_lds_dwordx4 v129, s[10:11]
	s_mov_b32 m0, s38
	s_add_i32 s12, s8, 3
	global_load_lds_dwordx4 v194, s[10:11]
	v_readlane_b32 s13, v248, s12
	s_mov_b32 m0, s39
	s_nop 1
	v_add_u32_e32 v194, s13, v206
	global_load_lds_dwordx4 v194, s[18:19]
	v_add_u32_e32 v194, s13, v213
	s_mov_b32 m0, s40
	s_nop 0
	global_load_lds_dwordx4 v194, s[18:19]
	s_mov_b32 m0, s41
	v_add_u32_e32 v194, 0x90000, v129
	global_load_lds_dwordx4 v194, s[10:11]
	v_add_u32_e32 v194, 0xd8000, v129
	s_mov_b32 m0, s42
	s_nop 0
	global_load_lds_dwordx4 v194, s[10:11]
	s_waitcnt vmcnt(8) lgkmcnt(0)
	s_barrier
	s_setprio 1
	v_mfma_f32_16x16x32_f16 v[12:15], v[130:133], v[146:149], v[12:15]
	v_mfma_f32_16x16x32_f16 v[12:15], v[134:137], v[150:153], v[12:15]
	v_mfma_f32_16x16x32_f16 v[8:11], v[138:141], v[146:149], v[8:11]
	v_mfma_f32_16x16x32_f16 v[8:11], v[142:145], v[150:153], v[8:11]
	v_mfma_f32_16x16x32_f16 v[64:67], v[178:181], v[146:149], v[64:67]
	v_mfma_f32_16x16x32_f16 v[64:67], v[182:185], v[150:153], v[64:67]
	v_mfma_f32_16x16x32_f16 v[68:71], v[186:189], v[146:149], v[68:71]
	v_mfma_f32_16x16x32_f16 v[68:71], v[190:193], v[150:153], v[68:71]
	v_mfma_f32_16x16x32_f16 v[4:7], v[130:133], v[154:157], v[4:7]
	v_mfma_f32_16x16x32_f16 v[4:7], v[134:137], v[158:161], v[4:7]
	v_mfma_f32_16x16x32_f16 v[0:3], v[138:141], v[154:157], v[0:3]
	v_mfma_f32_16x16x32_f16 v[0:3], v[142:145], v[158:161], v[0:3]
	v_mfma_f32_16x16x32_f16 v[72:75], v[178:181], v[154:157], v[72:75]
	v_mfma_f32_16x16x32_f16 v[72:75], v[182:185], v[158:161], v[72:75]
	v_mfma_f32_16x16x32_f16 v[76:79], v[186:189], v[154:157], v[76:79]
	v_mfma_f32_16x16x32_f16 v[76:79], v[190:193], v[158:161], v[76:79]
	v_mfma_f32_16x16x32_f16 v[44:47], v[130:133], v[162:165], v[44:47]
	v_mfma_f32_16x16x32_f16 v[44:47], v[134:137], v[166:169], v[44:47]
	v_mfma_f32_16x16x32_f16 v[48:51], v[138:141], v[162:165], v[48:51]
	v_mfma_f32_16x16x32_f16 v[48:51], v[142:145], v[166:169], v[48:51]
	v_mfma_f32_16x16x32_f16 v[80:83], v[178:181], v[162:165], v[80:83]
	v_mfma_f32_16x16x32_f16 v[80:83], v[182:185], v[166:169], v[80:83]
	v_mfma_f32_16x16x32_f16 v[84:87], v[186:189], v[162:165], v[84:87]
	v_mfma_f32_16x16x32_f16 v[84:87], v[190:193], v[166:169], v[84:87]
	v_mfma_f32_16x16x32_f16 v[56:59], v[130:133], v[170:173], v[56:59]
	v_mfma_f32_16x16x32_f16 v[56:59], v[134:137], v[174:177], v[56:59]
	v_mfma_f32_16x16x32_f16 v[60:63], v[138:141], v[170:173], v[60:63]
	v_mfma_f32_16x16x32_f16 v[60:63], v[142:145], v[174:177], v[60:63]
	v_mfma_f32_16x16x32_f16 v[88:91], v[178:181], v[170:173], v[88:91]
	v_mfma_f32_16x16x32_f16 v[88:91], v[182:185], v[174:177], v[88:91]
	v_mfma_f32_16x16x32_f16 v[92:95], v[186:189], v[170:173], v[92:95]
	v_mfma_f32_16x16x32_f16 v[92:95], v[190:193], v[174:177], v[92:95]
	s_setprio 0
	s_addk_i32 s7, 0x100
	s_cmp_lt_u32 s8, 32
	s_mov_b32 s8, s9
	s_barrier
.LBB1_82:
	ds_read_b128 v[130:133], v219 offset:32768
	ds_read_b128 v[134:137], v219 offset:33792
	ds_read_b128 v[138:141], v219 offset:34816
	ds_read_b128 v[142:145], v219 offset:35840
	ds_read_b128 v[178:181], v219 offset:49152
	ds_read_b128 v[182:185], v219 offset:50176
	ds_read_b128 v[186:189], v219 offset:51200
	ds_read_b128 v[190:193], v219 offset:52224
	ds_read_b128 v[146:149], v220
	ds_read_b128 v[150:153], v220 offset:1024
	ds_read_b128 v[154:157], v221
	ds_read_b128 v[158:161], v221 offset:1024
	ds_read_b128 v[162:165], v222
	ds_read_b128 v[166:169], v222 offset:1024
	ds_read_b128 v[170:173], v223
	ds_read_b128 v[174:177], v223 offset:1024
	s_add_i32 s12, s8, 1
	s_mov_b32 m0, s43
	v_readlane_b32 s9, v248, s12
	s_nop 1
	v_add_u32_e32 v251, s9, v249
	global_load_lds_dwordx4 v251, s[18:19]
	v_add_u32_e32 v251, s9, v250
	s_mov_b32 m0, s44
	s_nop 0
	global_load_lds_dwordx4 v251, s[18:19]
	s_waitcnt vmcnt(8) lgkmcnt(0)
	s_barrier
	s_setprio 1
	v_mfma_f32_16x16x32_f16 v[124:127], v[130:133], v[146:149], v[124:127]
	v_mfma_f32_16x16x32_f16 v[124:127], v[134:137], v[150:153], v[124:127]
	v_mfma_f32_16x16x32_f16 v[120:123], v[138:141], v[146:149], v[120:123]
	v_mfma_f32_16x16x32_f16 v[120:123], v[142:145], v[150:153], v[120:123]
	v_mfma_f32_16x16x32_f16 v[52:55], v[178:181], v[146:149], v[52:55]
	v_mfma_f32_16x16x32_f16 v[52:55], v[182:185], v[150:153], v[52:55]
	v_mfma_f32_16x16x32_f16 v[40:43], v[186:189], v[146:149], v[40:43]
	v_mfma_f32_16x16x32_f16 v[40:43], v[190:193], v[150:153], v[40:43]
	v_mfma_f32_16x16x32_f16 v[116:119], v[130:133], v[154:157], v[116:119]
	v_mfma_f32_16x16x32_f16 v[116:119], v[134:137], v[158:161], v[116:119]
	v_mfma_f32_16x16x32_f16 v[112:115], v[138:141], v[154:157], v[112:115]
	v_mfma_f32_16x16x32_f16 v[112:115], v[142:145], v[158:161], v[112:115]
	v_mfma_f32_16x16x32_f16 v[36:39], v[178:181], v[154:157], v[36:39]
	v_mfma_f32_16x16x32_f16 v[36:39], v[182:185], v[158:161], v[36:39]
	v_mfma_f32_16x16x32_f16 v[32:35], v[186:189], v[154:157], v[32:35]
	v_mfma_f32_16x16x32_f16 v[32:35], v[190:193], v[158:161], v[32:35]
	v_mfma_f32_16x16x32_f16 v[108:111], v[130:133], v[162:165], v[108:111]
	v_mfma_f32_16x16x32_f16 v[108:111], v[134:137], v[166:169], v[108:111]
	v_mfma_f32_16x16x32_f16 v[104:107], v[138:141], v[162:165], v[104:107]
	v_mfma_f32_16x16x32_f16 v[104:107], v[142:145], v[166:169], v[104:107]
	v_mfma_f32_16x16x32_f16 v[28:31], v[178:181], v[162:165], v[28:31]
	v_mfma_f32_16x16x32_f16 v[28:31], v[182:185], v[166:169], v[28:31]
	v_mfma_f32_16x16x32_f16 v[24:27], v[186:189], v[162:165], v[24:27]
	v_mfma_f32_16x16x32_f16 v[24:27], v[190:193], v[166:169], v[24:27]
	v_mfma_f32_16x16x32_f16 v[100:103], v[130:133], v[170:173], v[100:103]
	v_mfma_f32_16x16x32_f16 v[100:103], v[134:137], v[174:177], v[100:103]
	v_mfma_f32_16x16x32_f16 v[96:99], v[138:141], v[170:173], v[96:99]
	v_mfma_f32_16x16x32_f16 v[96:99], v[142:145], v[174:177], v[96:99]
	v_mfma_f32_16x16x32_f16 v[20:23], v[178:181], v[170:173], v[20:23]
	v_mfma_f32_16x16x32_f16 v[20:23], v[182:185], v[174:177], v[20:23]
	v_mfma_f32_16x16x32_f16 v[16:19], v[186:189], v[170:173], v[16:19]
	v_mfma_f32_16x16x32_f16 v[16:19], v[190:193], v[174:177], v[16:19]
	s_setprio 0
	s_barrier
	ds_read_b128 v[146:149], v220 offset:16384
	ds_read_b128 v[150:153], v220 offset:17408
	ds_read_b128 v[154:157], v221 offset:16384
	ds_read_b128 v[158:161], v221 offset:17408
	ds_read_b128 v[162:165], v222 offset:16384
	ds_read_b128 v[166:169], v222 offset:17408
	ds_read_b128 v[170:173], v223 offset:16384
	ds_read_b128 v[174:177], v223 offset:17408
	v_add_u32_e32 v129, s7, v128
	s_mov_b32 m0, s22
	v_add_u32_e32 v194, 0xffffff80, v129
	global_load_lds_dwordx4 v194, s[10:11]
	v_add_u32_e32 v194, 0x47f80, v129
	s_mov_b32 m0, s23
	s_add_i32 s9, s8, 2
	global_load_lds_dwordx4 v194, s[10:11]
	v_readlane_b32 s13, v248, s9
	s_mov_b32 m0, s21
	s_nop 1
	v_add_u32_e32 v194, s13, v206
	global_load_lds_dwordx4 v194, s[18:19]
	v_add_u32_e32 v194, s13, v213
	s_mov_b32 m0, s24
	s_nop 0
	global_load_lds_dwordx4 v194, s[18:19]
	s_mov_b32 m0, s25
	v_add_u32_e32 v194, 0x8ff80, v129
	global_load_lds_dwordx4 v194, s[10:11]
	v_add_u32_e32 v194, 0xd7f80, v129
	s_mov_b32 m0, s26
	s_nop 0
	global_load_lds_dwordx4 v194, s[10:11]
	s_waitcnt vmcnt(8) lgkmcnt(0)
	s_barrier
	s_setprio 1
	v_mfma_f32_16x16x32_f16 v[12:15], v[130:133], v[146:149], v[12:15]
	v_mfma_f32_16x16x32_f16 v[12:15], v[134:137], v[150:153], v[12:15]
	v_mfma_f32_16x16x32_f16 v[8:11], v[138:141], v[146:149], v[8:11]
	v_mfma_f32_16x16x32_f16 v[8:11], v[142:145], v[150:153], v[8:11]
	v_mfma_f32_16x16x32_f16 v[64:67], v[178:181], v[146:149], v[64:67]
	v_mfma_f32_16x16x32_f16 v[64:67], v[182:185], v[150:153], v[64:67]
	v_mfma_f32_16x16x32_f16 v[68:71], v[186:189], v[146:149], v[68:71]
	v_mfma_f32_16x16x32_f16 v[68:71], v[190:193], v[150:153], v[68:71]
	v_mfma_f32_16x16x32_f16 v[4:7], v[130:133], v[154:157], v[4:7]
	v_mfma_f32_16x16x32_f16 v[4:7], v[134:137], v[158:161], v[4:7]
	v_mfma_f32_16x16x32_f16 v[0:3], v[138:141], v[154:157], v[0:3]
	v_mfma_f32_16x16x32_f16 v[0:3], v[142:145], v[158:161], v[0:3]
	v_mfma_f32_16x16x32_f16 v[72:75], v[178:181], v[154:157], v[72:75]
	v_mfma_f32_16x16x32_f16 v[72:75], v[182:185], v[158:161], v[72:75]
	v_mfma_f32_16x16x32_f16 v[76:79], v[186:189], v[154:157], v[76:79]
	v_mfma_f32_16x16x32_f16 v[76:79], v[190:193], v[158:161], v[76:79]
	v_mfma_f32_16x16x32_f16 v[44:47], v[130:133], v[162:165], v[44:47]
	v_mfma_f32_16x16x32_f16 v[44:47], v[134:137], v[166:169], v[44:47]
	v_mfma_f32_16x16x32_f16 v[48:51], v[138:141], v[162:165], v[48:51]
	v_mfma_f32_16x16x32_f16 v[48:51], v[142:145], v[166:169], v[48:51]
	v_mfma_f32_16x16x32_f16 v[80:83], v[178:181], v[162:165], v[80:83]
	v_mfma_f32_16x16x32_f16 v[80:83], v[182:185], v[166:169], v[80:83]
	v_mfma_f32_16x16x32_f16 v[84:87], v[186:189], v[162:165], v[84:87]
	v_mfma_f32_16x16x32_f16 v[84:87], v[190:193], v[166:169], v[84:87]
	v_mfma_f32_16x16x32_f16 v[56:59], v[130:133], v[170:173], v[56:59]
	v_mfma_f32_16x16x32_f16 v[56:59], v[134:137], v[174:177], v[56:59]
	v_mfma_f32_16x16x32_f16 v[60:63], v[138:141], v[170:173], v[60:63]
	v_mfma_f32_16x16x32_f16 v[60:63], v[142:145], v[174:177], v[60:63]
	v_mfma_f32_16x16x32_f16 v[88:91], v[178:181], v[170:173], v[88:91]
	v_mfma_f32_16x16x32_f16 v[88:91], v[182:185], v[174:177], v[88:91]
	v_mfma_f32_16x16x32_f16 v[92:95], v[186:189], v[170:173], v[92:95]
	v_mfma_f32_16x16x32_f16 v[92:95], v[190:193], v[174:177], v[92:95]
	s_setprio 0
	s_barrier
	ds_read_b128 v[130:133], v224
	ds_read_b128 v[134:137], v224 offset:1024
	ds_read_b128 v[138:141], v224 offset:2048
	ds_read_b128 v[142:145], v224 offset:3072
	ds_read_b128 v[178:181], v229
	ds_read_b128 v[182:185], v229 offset:1024
	ds_read_b128 v[186:189], v229 offset:2048
	ds_read_b128 v[190:193], v229 offset:3072
	ds_read_b128 v[146:149], v225
	ds_read_b128 v[150:153], v225 offset:1024
	ds_read_b128 v[154:157], v226
	ds_read_b128 v[158:161], v226 offset:1024
	ds_read_b128 v[162:165], v227
	ds_read_b128 v[166:169], v227 offset:1024
	ds_read_b128 v[170:173], v228
	ds_read_b128 v[174:177], v228 offset:1024
	v_readlane_b32 s12, v248, s9
	s_mov_b32 m0, s27
	s_nop 1
	v_add_u32_e32 v251, s12, v249
	global_load_lds_dwordx4 v251, s[18:19]
	v_add_u32_e32 v251, s12, v250
	s_mov_b32 m0, s28
	s_nop 0
	global_load_lds_dwordx4 v251, s[18:19]
	s_waitcnt vmcnt(8) lgkmcnt(0)
	s_barrier
	s_setprio 1
	v_mfma_f32_16x16x32_f16 v[124:127], v[130:133], v[146:149], v[124:127]
	v_mfma_f32_16x16x32_f16 v[124:127], v[134:137], v[150:153], v[124:127]
	v_mfma_f32_16x16x32_f16 v[120:123], v[138:141], v[146:149], v[120:123]
	v_mfma_f32_16x16x32_f16 v[120:123], v[142:145], v[150:153], v[120:123]
	v_mfma_f32_16x16x32_f16 v[52:55], v[178:181], v[146:149], v[52:55]
	v_mfma_f32_16x16x32_f16 v[52:55], v[182:185], v[150:153], v[52:55]
	v_mfma_f32_16x16x32_f16 v[40:43], v[186:189], v[146:149], v[40:43]
	v_mfma_f32_16x16x32_f16 v[40:43], v[190:193], v[150:153], v[40:43]
	v_mfma_f32_16x16x32_f16 v[116:119], v[130:133], v[154:157], v[116:119]
	v_mfma_f32_16x16x32_f16 v[116:119], v[134:137], v[158:161], v[116:119]
	v_mfma_f32_16x16x32_f16 v[112:115], v[138:141], v[154:157], v[112:115]
	v_mfma_f32_16x16x32_f16 v[112:115], v[142:145], v[158:161], v[112:115]
	v_mfma_f32_16x16x32_f16 v[36:39], v[178:181], v[154:157], v[36:39]
	v_mfma_f32_16x16x32_f16 v[36:39], v[182:185], v[158:161], v[36:39]
	v_mfma_f32_16x16x32_f16 v[32:35], v[186:189], v[154:157], v[32:35]
	v_mfma_f32_16x16x32_f16 v[32:35], v[190:193], v[158:161], v[32:35]
	v_mfma_f32_16x16x32_f16 v[108:111], v[130:133], v[162:165], v[108:111]
	v_mfma_f32_16x16x32_f16 v[108:111], v[134:137], v[166:169], v[108:111]
	v_mfma_f32_16x16x32_f16 v[104:107], v[138:141], v[162:165], v[104:107]
	v_mfma_f32_16x16x32_f16 v[104:107], v[142:145], v[166:169], v[104:107]
	v_mfma_f32_16x16x32_f16 v[28:31], v[178:181], v[162:165], v[28:31]
	v_mfma_f32_16x16x32_f16 v[28:31], v[182:185], v[166:169], v[28:31]
	v_mfma_f32_16x16x32_f16 v[24:27], v[186:189], v[162:165], v[24:27]
	v_mfma_f32_16x16x32_f16 v[24:27], v[190:193], v[166:169], v[24:27]
	v_mfma_f32_16x16x32_f16 v[100:103], v[130:133], v[170:173], v[100:103]
	v_mfma_f32_16x16x32_f16 v[100:103], v[134:137], v[174:177], v[100:103]
	v_mfma_f32_16x16x32_f16 v[96:99], v[138:141], v[170:173], v[96:99]
	v_mfma_f32_16x16x32_f16 v[96:99], v[142:145], v[174:177], v[96:99]
	v_mfma_f32_16x16x32_f16 v[20:23], v[178:181], v[170:173], v[20:23]
	v_mfma_f32_16x16x32_f16 v[20:23], v[182:185], v[174:177], v[20:23]
	v_mfma_f32_16x16x32_f16 v[16:19], v[186:189], v[170:173], v[16:19]
	v_mfma_f32_16x16x32_f16 v[16:19], v[190:193], v[174:177], v[16:19]
	s_setprio 0
	s_barrier
	ds_read_b128 v[146:149], v230
	ds_read_b128 v[150:153], v230 offset:1024
	ds_read_b128 v[154:157], v231
	ds_read_b128 v[158:161], v231 offset:1024
	ds_read_b128 v[162:165], v232
	ds_read_b128 v[166:169], v232 offset:1024
	ds_read_b128 v[170:173], v233
	ds_read_b128 v[174:177], v233 offset:1024
	s_mov_b32 m0, s37
	v_add_u32_e32 v194, 0x48000, v129
	global_load_lds_dwordx4 v129, s[10:11]
	s_mov_b32 m0, s38
	s_add_i32 s12, s8, 3
	global_load_lds_dwordx4 v194, s[10:11]
	v_readlane_b32 s13, v248, s12
	s_mov_b32 m0, s39
	s_nop 1
	v_add_u32_e32 v194, s13, v206
	global_load_lds_dwordx4 v194, s[18:19]
	v_add_u32_e32 v194, s13, v213
	s_mov_b32 m0, s40
	s_nop 0
	global_load_lds_dwordx4 v194, s[18:19]
	s_mov_b32 m0, s41
	v_add_u32_e32 v194, 0x90000, v129
	global_load_lds_dwordx4 v194, s[10:11]
	v_add_u32_e32 v194, 0xd8000, v129
	s_mov_b32 m0, s42
	s_nop 0
	global_load_lds_dwordx4 v194, s[10:11]
	s_waitcnt vmcnt(8) lgkmcnt(0)
	s_barrier
	s_setprio 1
	v_mfma_f32_16x16x32_f16 v[12:15], v[130:133], v[146:149], v[12:15]
	v_mfma_f32_16x16x32_f16 v[12:15], v[134:137], v[150:153], v[12:15]
	v_mfma_f32_16x16x32_f16 v[8:11], v[138:141], v[146:149], v[8:11]
	v_mfma_f32_16x16x32_f16 v[8:11], v[142:145], v[150:153], v[8:11]
	v_mfma_f32_16x16x32_f16 v[64:67], v[178:181], v[146:149], v[64:67]
	v_mfma_f32_16x16x32_f16 v[64:67], v[182:185], v[150:153], v[64:67]
	v_mfma_f32_16x16x32_f16 v[68:71], v[186:189], v[146:149], v[68:71]
	v_mfma_f32_16x16x32_f16 v[68:71], v[190:193], v[150:153], v[68:71]
	v_mfma_f32_16x16x32_f16 v[4:7], v[130:133], v[154:157], v[4:7]
	v_mfma_f32_16x16x32_f16 v[4:7], v[134:137], v[158:161], v[4:7]
	v_mfma_f32_16x16x32_f16 v[0:3], v[138:141], v[154:157], v[0:3]
	v_mfma_f32_16x16x32_f16 v[0:3], v[142:145], v[158:161], v[0:3]
	v_mfma_f32_16x16x32_f16 v[72:75], v[178:181], v[154:157], v[72:75]
	v_mfma_f32_16x16x32_f16 v[72:75], v[182:185], v[158:161], v[72:75]
	v_mfma_f32_16x16x32_f16 v[76:79], v[186:189], v[154:157], v[76:79]
	v_mfma_f32_16x16x32_f16 v[76:79], v[190:193], v[158:161], v[76:79]
	v_mfma_f32_16x16x32_f16 v[44:47], v[130:133], v[162:165], v[44:47]
	v_mfma_f32_16x16x32_f16 v[44:47], v[134:137], v[166:169], v[44:47]
	v_mfma_f32_16x16x32_f16 v[48:51], v[138:141], v[162:165], v[48:51]
	v_mfma_f32_16x16x32_f16 v[48:51], v[142:145], v[166:169], v[48:51]
	v_mfma_f32_16x16x32_f16 v[80:83], v[178:181], v[162:165], v[80:83]
	v_mfma_f32_16x16x32_f16 v[80:83], v[182:185], v[166:169], v[80:83]
	v_mfma_f32_16x16x32_f16 v[84:87], v[186:189], v[162:165], v[84:87]
	v_mfma_f32_16x16x32_f16 v[84:87], v[190:193], v[166:169], v[84:87]
	v_mfma_f32_16x16x32_f16 v[56:59], v[130:133], v[170:173], v[56:59]
	v_mfma_f32_16x16x32_f16 v[56:59], v[134:137], v[174:177], v[56:59]
	v_mfma_f32_16x16x32_f16 v[60:63], v[138:141], v[170:173], v[60:63]
	v_mfma_f32_16x16x32_f16 v[60:63], v[142:145], v[174:177], v[60:63]
	v_mfma_f32_16x16x32_f16 v[88:91], v[178:181], v[170:173], v[88:91]
	v_mfma_f32_16x16x32_f16 v[88:91], v[182:185], v[174:177], v[88:91]
	v_mfma_f32_16x16x32_f16 v[92:95], v[186:189], v[170:173], v[92:95]
	v_mfma_f32_16x16x32_f16 v[92:95], v[190:193], v[174:177], v[92:95]
	s_setprio 0
	s_addk_i32 s7, 0x100
	s_cmp_lt_u32 s8, 32
	s_mov_b32 s8, s9
	s_barrier
	s_cbranch_scc1 .LBB1_82
	ds_read_b128 v[132:135], v219 offset:32768
	ds_read_b128 v[136:139], v219 offset:33792
	ds_read_b128 v[140:143], v219 offset:34816
	ds_read_b128 v[144:147], v219 offset:35840
	ds_read_b128 v[128:131], v220
	ds_read_b128 v[148:151], v220 offset:1024
	ds_read_b128 v[152:155], v221
	ds_read_b128 v[156:159], v221 offset:1024
	ds_read_b128 v[188:191], v222
	ds_read_b128 v[192:195], v222 offset:1024
	ds_read_b128 v[196:199], v223
	ds_read_b128 v[200:203], v223 offset:1024
	s_setprio 2
	s_lshl_b32 s3, s50, 9
	s_add_i32 s3, s47, s3
	s_add_i32 s3, s3, 0x10380
	s_mov_b32 m0, s43
	v_add_u32_e32 v160, s3, v206
	global_load_lds_dwordx4 v160, s[18:19]
	v_add_u32_e32 v160, s3, v213
	s_mov_b32 m0, s44
	s_nop 0
	global_load_lds_dwordx4 v160, s[18:19]
	s_setprio 0
	s_waitcnt vmcnt(8)
	s_waitcnt lgkmcnt(0)
	s_barrier
	s_waitcnt lgkmcnt(0)
	s_setprio 1
	s_waitcnt lgkmcnt(0)
	v_mfma_f32_16x16x32_f16 v[124:127], v[132:135], v[128:131], v[124:127]
	v_mfma_f32_16x16x32_f16 v[120:123], v[140:143], v[128:131], v[120:123]
	v_mfma_f32_16x16x32_f16 v[116:119], v[132:135], v[152:155], v[116:119]
	v_mfma_f32_16x16x32_f16 v[112:115], v[140:143], v[152:155], v[112:115]
	v_mfma_f32_16x16x32_f16 v[108:111], v[132:135], v[188:191], v[108:111]
	v_mfma_f32_16x16x32_f16 v[104:107], v[140:143], v[188:191], v[104:107]
	v_mfma_f32_16x16x32_f16 v[100:103], v[132:135], v[196:199], v[100:103]
	v_mfma_f32_16x16x32_f16 v[96:99], v[140:143], v[196:199], v[96:99]
	v_mfma_f32_16x16x32_f16 v[160:163], v[136:139], v[148:151], v[124:127]
	v_mfma_f32_16x16x32_f16 v[164:167], v[144:147], v[148:151], v[120:123]
	v_mfma_f32_16x16x32_f16 v[168:171], v[136:139], v[156:159], v[116:119]
	v_mfma_f32_16x16x32_f16 v[172:175], v[144:147], v[156:159], v[112:115]
	v_mfma_f32_16x16x32_f16 v[176:179], v[136:139], v[192:195], v[108:111]
	v_mfma_f32_16x16x32_f16 v[180:183], v[144:147], v[192:195], v[104:107]
	v_mfma_f32_16x16x32_f16 v[100:103], v[136:139], v[200:203], v[100:103]
	v_mfma_f32_16x16x32_f16 v[184:187], v[144:147], v[200:203], v[96:99]
	s_setprio 0
	s_barrier
	ds_read_b128 v[104:107], v219 offset:49152
	ds_read_b128 v[108:111], v219 offset:50176
	ds_read_b128 v[116:119], v219 offset:51200
	ds_read_b128 v[236:239], v219 offset:52224
	s_waitcnt lgkmcnt(0)
	s_barrier
	s_waitcnt lgkmcnt(0)
	s_setprio 1
	s_waitcnt lgkmcnt(0)
	v_mfma_f32_16x16x32_f16 v[52:55], v[104:107], v[128:131], v[52:55]
	v_mfma_f32_16x16x32_f16 v[40:43], v[116:119], v[128:131], v[40:43]
	v_mfma_f32_16x16x32_f16 v[36:39], v[104:107], v[152:155], v[36:39]
	v_mfma_f32_16x16x32_f16 v[32:35], v[116:119], v[152:155], v[32:35]
	v_mfma_f32_16x16x32_f16 v[28:31], v[104:107], v[188:191], v[28:31]
	v_mfma_f32_16x16x32_f16 v[24:27], v[116:119], v[188:191], v[24:27]
	v_mfma_f32_16x16x32_f16 v[20:23], v[104:107], v[196:199], v[20:23]
	v_mfma_f32_16x16x32_f16 v[16:19], v[116:119], v[196:199], v[16:19]
	v_mfma_f32_16x16x32_f16 v[52:55], v[108:111], v[148:151], v[52:55]
	v_mfma_f32_16x16x32_f16 v[40:43], v[236:239], v[148:151], v[40:43]
	v_mfma_f32_16x16x32_f16 v[36:39], v[108:111], v[156:159], v[36:39]
	v_mfma_f32_16x16x32_f16 v[32:35], v[236:239], v[156:159], v[32:35]
	v_mfma_f32_16x16x32_f16 v[28:31], v[108:111], v[192:195], v[28:31]
	v_mfma_f32_16x16x32_f16 v[24:27], v[236:239], v[192:195], v[24:27]
	v_mfma_f32_16x16x32_f16 v[96:99], v[108:111], v[200:203], v[20:23]
	v_mfma_f32_16x16x32_f16 v[16:19], v[236:239], v[200:203], v[16:19]
	s_setprio 0
	s_barrier
	ds_read_b128 v[20:23], v220 offset:16384
	ds_read_b128 v[148:151], v220 offset:17408
	ds_read_b128 v[152:155], v221 offset:16384
	ds_read_b128 v[156:159], v221 offset:17408
	ds_read_b128 v[188:191], v222 offset:16384
	ds_read_b128 v[192:195], v222 offset:17408
	ds_read_b128 v[196:199], v223 offset:16384
	ds_read_b128 v[200:203], v223 offset:17408
	s_waitcnt vmcnt(4)
	s_waitcnt lgkmcnt(0)
	s_barrier
	s_waitcnt lgkmcnt(0)
	s_setprio 1
	s_waitcnt lgkmcnt(0)
	v_mfma_f32_16x16x32_f16 v[0:3], v[140:143], v[152:155], v[0:3]
	v_mfma_f32_16x16x32_f16 v[124:127], v[144:147], v[156:159], v[0:3]
	v_mfma_f32_16x16x32_f16 v[0:3], v[132:135], v[188:191], v[44:47]
	v_mfma_f32_16x16x32_f16 v[128:131], v[136:139], v[192:195], v[0:3]
	v_mfma_f32_16x16x32_f16 v[0:3], v[140:143], v[188:191], v[48:51]
	v_mfma_f32_16x16x32_f16 v[48:51], v[144:147], v[192:195], v[0:3]
	v_mfma_f32_16x16x32_f16 v[0:3], v[132:135], v[196:199], v[56:59]
	v_mfma_f32_16x16x32_f16 v[12:15], v[132:135], v[20:23], v[12:15]
	v_mfma_f32_16x16x32_f16 v[8:11], v[140:143], v[20:23], v[8:11]
	v_mfma_f32_16x16x32_f16 v[4:7], v[132:135], v[152:155], v[4:7]
	v_mfma_f32_16x16x32_f16 v[56:59], v[136:139], v[200:203], v[0:3]
	v_mfma_f32_16x16x32_f16 v[0:3], v[140:143], v[196:199], v[60:63]
	v_mfma_f32_16x16x32_f16 v[112:115], v[136:139], v[148:151], v[12:15]
	v_mfma_f32_16x16x32_f16 v[8:11], v[144:147], v[148:151], v[8:11]
	v_mfma_f32_16x16x32_f16 v[120:123], v[136:139], v[156:159], v[4:7]
	v_mfma_f32_16x16x32_f16 v[60:63], v[144:147], v[200:203], v[0:3]
	s_setprio 0
	s_setprio 1
	v_mfma_f32_16x16x32_f16 v[0:3], v[104:107], v[20:23], v[64:67]
	v_mfma_f32_16x16x32_f16 v[132:135], v[108:111], v[148:151], v[0:3]
	v_mfma_f32_16x16x32_f16 v[0:3], v[116:119], v[20:23], v[68:71]
	v_mfma_f32_16x16x32_f16 v[136:139], v[236:239], v[148:151], v[0:3]
	v_mfma_f32_16x16x32_f16 v[0:3], v[104:107], v[152:155], v[72:75]
	v_mfma_f32_16x16x32_f16 v[140:143], v[108:111], v[156:159], v[0:3]
	v_mfma_f32_16x16x32_f16 v[0:3], v[116:119], v[152:155], v[76:79]
	v_mfma_f32_16x16x32_f16 v[144:147], v[236:239], v[156:159], v[0:3]
	v_mfma_f32_16x16x32_f16 v[0:3], v[104:107], v[188:191], v[80:83]
	v_mfma_f32_16x16x32_f16 v[80:83], v[108:111], v[192:195], v[0:3]
	v_mfma_f32_16x16x32_f16 v[0:3], v[116:119], v[188:191], v[84:87]
	v_mfma_f32_16x16x32_f16 v[148:151], v[236:239], v[192:195], v[0:3]
	v_mfma_f32_16x16x32_f16 v[0:3], v[104:107], v[196:199], v[88:91]
	v_mfma_f32_16x16x32_f16 v[152:155], v[108:111], v[200:203], v[0:3]
	v_mfma_f32_16x16x32_f16 v[0:3], v[116:119], v[196:199], v[92:95]
	v_mfma_f32_16x16x32_f16 v[156:159], v[236:239], v[200:203], v[0:3]
	s_setprio 0
	s_add_i32 s49, s49, s17
	s_cmpk_lt_i32 s49, 0x1c8
	s_cselect_b64 s[6:7], -1, 0
	s_cmpk_gt_i32 s49, 0x1c7
	s_cselect_b64 s[12:13], -1, 0
	s_and_b64 vcc, exec, s[12:13]
	s_mov_b32 s54, s2
	s_mov_b32 s53, s51
	s_mov_b32 s55, s52
	s_barrier
	s_cbranch_vccnz .LBB1_100
	s_cmpk_lt_i32 s49, 0x148
	s_cbranch_scc1 .LBB1_88
	s_cmpk_lt_u32 s49, 0x1a0
	s_cbranch_scc1 .LBB1_89
	s_cmpk_lt_u32 s49, 0x1b8
	s_cbranch_scc1 .LBB1_90
	s_cmpk_lt_u32 s49, 0x1c0
	s_cselect_b32 s47, s45, 0xfffffe40
	s_cselect_b32 s48, 3, 4
	s_mov_b32 s3, 1
	s_cmp_lt_i32 s48, 1
	s_movk_i32 s53, 0x64
	s_cbranch_scc0 .LBB1_91
	s_branch .LBB1_99
